# P7 w_down queue: hand-written grab body and the wait for the next grab's atomic deferred to the end of the grab (no atomic round trip before wave 0's loads)
# speedup vs baseline: 1.0029x; 1.0029x over previous
.LBB0_1054:
	s_or_b64 exec, exec, s[14:15]
	s_waitcnt lgkmcnt(0)
	s_barrier
	s_waitcnt vmcnt(5)
	ds_read_b32 v0, v135
	s_waitcnt lgkmcnt(0)
	s_barrier
	v_readfirstlane_b32 s26, v0
	s_cmpk_gt_i32 s26, 0x38ff
	s_cselect_b64 s[14:15], -1, 0
	s_and_b64 vcc, exec, s[14:15]
	s_cbranch_vccnz .LBB0_1051
	s_mov_b64 s[16:17], exec
	v_readlane_b32 s18, v255, 24
	v_readlane_b32 s19, v255, 25
	s_and_b64 s[18:19], s[16:17], s[18:19]
	s_mov_b64 exec, s[18:19]
	s_cbranch_execz .LBB0_1059
	s_mov_b64 s[20:21], exec
	v_mbcnt_lo_u32_b32 v0, s20, 0
	v_mbcnt_hi_u32_b32 v0, s21, v0
	v_cmp_eq_u32_e32 vcc, 0, v0
	s_and_saveexec_b64 s[18:19], vcc
	s_cbranch_execz .LBB0_1058
	s_bcnt1_i32_b64 s12, s[20:21]
	s_lshl_b32 s12, s12, 4
	v_mov_b32_e32 v156, s12
	global_atomic_add v156, v129, v156, s[8:9] sc0

.LBB0_1059:
	s_or_b64 exec, exec, s[16:17]
	s_and_b64 vcc, exec, s[4:5]
	s_cbranch_vccnz .LBB0_1051
	v_readlane_b32 s12, v255, 28
	s_add_i32 s16, s26, s12
	s_add_i32 s19, s16, 0
	s_and_b32 s20, s19, 1
	s_lshl_b32 s20, s20, 6
	s_and_b32 s21, s19, 0x7e
	s_lshr_b32 s21, s21, 1
	s_andn2_b32 s19, s19, 0x7f
	s_or_b32 s19, s19, s20
	s_or_b32 s19, s19, s21
	s_add_i32 s17, s19, 0x4000
	s_add_i32 s19, s16, 8
	s_and_b32 s20, s19, 1
	s_lshl_b32 s20, s20, 6
	s_and_b32 s21, s19, 0x7e
	s_lshr_b32 s21, s21, 1
	s_andn2_b32 s19, s19, 0x7f
	s_or_b32 s19, s19, s20
	s_or_b32 s19, s19, s21
	s_add_i32 s18, s19, 0x4000
	v_mbcnt_lo_u32_b32 v154, -1, 0
	v_mbcnt_hi_u32_b32 v154, -1, v154
	v_lshrrev_b32_e32 v155, 3, v154
	v_and_b32_e32 v154, 7, v154
	v_lshlrev_b32_e32 v152, 17, v155
	v_lshl_or_b32 v152, v154, 4, v152
	v_lshlrev_b32_e32 v153, 13, v154
	v_lshl_or_b32 v153, v155, 4, v153
	s_mov_b32 s36, 0x44000000
	s_lshr_b32 s19, s17, 10
	s_and_b32 s20, s17, 0x3ff
	s_lshr_b32 s21, s20, 6
	s_and_b32 s20, s20, 63
	s_lshl_b32 s22, s19, 24
	s_lshl_b32 s27, s21, 20
	s_add_i32 s22, s22, s27
	s_lshl_b32 s27, s20, 7
	s_add_i32 s22, s22, s27
	s_add_u32 s24, s70, s22
	s_addc_u32 s25, s71, 0
	global_load_dwordx4 v[0:3], v152, s[24:25] sc1 nt
	s_add_u32 s28, s24, 0x2000
	s_addc_u32 s29, s25, 0
	global_load_dwordx4 v[4:7], v152, s[28:29] sc1 nt
	s_add_u32 s28, s24, 0x4000
	s_addc_u32 s29, s25, 0
	global_load_dwordx4 v[8:11], v152, s[28:29] sc1 nt
	s_add_u32 s28, s24, 0x6000
	s_addc_u32 s29, s25, 0
	global_load_dwordx4 v[12:15], v152, s[28:29] sc1 nt
	s_add_u32 s28, s24, 0x8000
	s_addc_u32 s29, s25, 0
	global_load_dwordx4 v[16:19], v152, s[28:29] sc1 nt
	s_add_u32 s28, s24, 0xa000
	s_addc_u32 s29, s25, 0
	global_load_dwordx4 v[20:23], v152, s[28:29] sc1 nt
	s_add_u32 s28, s24, 0xc000
	s_addc_u32 s29, s25, 0
	global_load_dwordx4 v[24:27], v152, s[28:29] sc1 nt
	s_add_u32 s28, s24, 0xe000
	s_addc_u32 s29, s25, 0
	global_load_dwordx4 v[28:31], v152, s[28:29] sc1 nt
	s_add_u32 s28, s24, 0x10000
	s_addc_u32 s29, s25, 0
	global_load_dwordx4 v[32:35], v152, s[28:29] sc1 nt
	s_add_u32 s28, s24, 0x12000
	s_addc_u32 s29, s25, 0
	global_load_dwordx4 v[36:39], v152, s[28:29] sc1 nt
	s_add_u32 s28, s24, 0x14000
	s_addc_u32 s29, s25, 0
	global_load_dwordx4 v[40:43], v152, s[28:29] sc1 nt
	s_add_u32 s28, s24, 0x16000
	s_addc_u32 s29, s25, 0
	global_load_dwordx4 v[44:47], v152, s[28:29] sc1 nt
	s_add_u32 s28, s24, 0x18000
	s_addc_u32 s29, s25, 0
	global_load_dwordx4 v[48:51], v152, s[28:29] sc1 nt
	s_add_u32 s28, s24, 0x1a000
	s_addc_u32 s29, s25, 0
	global_load_dwordx4 v[52:55], v152, s[28:29] sc1 nt
	s_add_u32 s28, s24, 0x1c000
	s_addc_u32 s29, s25, 0
	global_load_dwordx4 v[56:59], v152, s[28:29] sc1 nt
	s_add_u32 s28, s24, 0x1e000
	s_addc_u32 s29, s25, 0
	global_load_dwordx4 v[60:63], v152, s[28:29] sc1 nt
	s_lshr_b32 s19, s18, 10
	s_and_b32 s20, s18, 0x3ff
	s_lshr_b32 s21, s20, 6
	s_and_b32 s20, s20, 63
	s_lshl_b32 s22, s19, 24
	s_lshl_b32 s27, s21, 20
	s_add_i32 s22, s22, s27
	s_lshl_b32 s27, s20, 7
	s_add_i32 s22, s22, s27
	s_add_u32 s24, s70, s22
	s_addc_u32 s25, s71, 0
	global_load_dwordx4 v[64:67], v152, s[24:25] sc1 nt
	s_add_u32 s28, s24, 0x2000
	s_addc_u32 s29, s25, 0
	global_load_dwordx4 v[68:71], v152, s[28:29] sc1 nt
	s_add_u32 s28, s24, 0x4000
	s_addc_u32 s29, s25, 0
	global_load_dwordx4 v[72:75], v152, s[28:29] sc1 nt
	s_add_u32 s28, s24, 0x6000
	s_addc_u32 s29, s25, 0
	global_load_dwordx4 v[76:79], v152, s[28:29] sc1 nt
	s_add_u32 s28, s24, 0x8000
	s_addc_u32 s29, s25, 0
	global_load_dwordx4 v[80:83], v152, s[28:29] sc1 nt
	s_add_u32 s28, s24, 0xa000
	s_addc_u32 s29, s25, 0
	global_load_dwordx4 v[84:87], v152, s[28:29] sc1 nt
	s_add_u32 s28, s24, 0xc000
	s_addc_u32 s29, s25, 0
	global_load_dwordx4 v[88:91], v152, s[28:29] sc1 nt
	s_add_u32 s28, s24, 0xe000
	s_addc_u32 s29, s25, 0
	global_load_dwordx4 v[92:95], v152, s[28:29] sc1 nt
	s_add_u32 s28, s24, 0x10000
	s_addc_u32 s29, s25, 0
	global_load_dwordx4 v[96:99], v152, s[28:29] sc1 nt
	s_add_u32 s28, s24, 0x12000
	s_addc_u32 s29, s25, 0
	global_load_dwordx4 v[100:103], v152, s[28:29] sc1 nt
	s_add_u32 s28, s24, 0x14000
	s_addc_u32 s29, s25, 0
	global_load_dwordx4 v[104:107], v152, s[28:29] sc1 nt
	s_add_u32 s28, s24, 0x16000
	s_addc_u32 s29, s25, 0
	global_load_dwordx4 v[108:111], v152, s[28:29] sc1 nt
	s_add_u32 s28, s24, 0x18000
	s_addc_u32 s29, s25, 0
	global_load_dwordx4 v[112:115], v152, s[28:29] sc1 nt
	s_add_u32 s28, s24, 0x1a000
	s_addc_u32 s29, s25, 0
	global_load_dwordx4 v[116:119], v152, s[28:29] sc1 nt
	s_add_u32 s28, s24, 0x1c000
	s_addc_u32 s29, s25, 0
	global_load_dwordx4 v[120:123], v152, s[28:29] sc1 nt
	s_add_u32 s28, s24, 0x1e000
	s_addc_u32 s29, s25, 0
	global_load_dwordx4 v[124:127], v152, s[28:29] sc1 nt
	s_waitcnt vmcnt(16)
	s_lshr_b32 s19, s17, 10
	s_and_b32 s20, s17, 0x3ff
	s_lshr_b32 s21, s20, 6
	s_and_b32 s20, s20, 63
	s_lshl_b32 s22, s19, 22
	s_lshl_b32 s27, s20, 16
	s_add_i32 s22, s22, s27
	s_lshl_b32 s27, s21, 7
	s_add_i32 s22, s22, s27
	s_add_u32 s30, s90, s22
	s_addc_u32 s31, s91, 0
	s_add_u32 s30, s30, 0x3b100000
	s_addc_u32 s31, s31, 0
	s_add_u32 s34, s30, 0x1000
	s_addc_u32 s35, s31, 0
	v_pk_mul_f32 v[0:1], v[0:1], s[36:37] op_sel_hi:[1,0]
	v_pk_mul_f32 v[2:3], v[2:3], s[36:37] op_sel_hi:[1,0]
	v_pk_mul_f32 v[4:5], v[4:5], s[36:37] op_sel_hi:[1,0]
	v_pk_mul_f32 v[6:7], v[6:7], s[36:37] op_sel_hi:[1,0]
	v_pk_mul_f32 v[8:9], v[8:9], s[36:37] op_sel_hi:[1,0]
	v_pk_mul_f32 v[10:11], v[10:11], s[36:37] op_sel_hi:[1,0]
	v_pk_mul_f32 v[12:13], v[12:13], s[36:37] op_sel_hi:[1,0]
	v_pk_mul_f32 v[14:15], v[14:15], s[36:37] op_sel_hi:[1,0]
	v_pk_mul_f32 v[16:17], v[16:17], s[36:37] op_sel_hi:[1,0]
	v_pk_mul_f32 v[18:19], v[18:19], s[36:37] op_sel_hi:[1,0]
	v_pk_mul_f32 v[20:21], v[20:21], s[36:37] op_sel_hi:[1,0]
	v_pk_mul_f32 v[22:23], v[22:23], s[36:37] op_sel_hi:[1,0]
	v_pk_mul_f32 v[24:25], v[24:25], s[36:37] op_sel_hi:[1,0]
	v_pk_mul_f32 v[26:27], v[26:27], s[36:37] op_sel_hi:[1,0]
	v_pk_mul_f32 v[28:29], v[28:29], s[36:37] op_sel_hi:[1,0]
	v_pk_mul_f32 v[30:31], v[30:31], s[36:37] op_sel_hi:[1,0]
	v_pk_mul_f32 v[32:33], v[32:33], s[36:37] op_sel_hi:[1,0]
	v_pk_mul_f32 v[34:35], v[34:35], s[36:37] op_sel_hi:[1,0]
	v_pk_mul_f32 v[36:37], v[36:37], s[36:37] op_sel_hi:[1,0]
	v_pk_mul_f32 v[38:39], v[38:39], s[36:37] op_sel_hi:[1,0]
	v_pk_mul_f32 v[40:41], v[40:41], s[36:37] op_sel_hi:[1,0]
	v_pk_mul_f32 v[42:43], v[42:43], s[36:37] op_sel_hi:[1,0]
	v_pk_mul_f32 v[44:45], v[44:45], s[36:37] op_sel_hi:[1,0]
	v_pk_mul_f32 v[46:47], v[46:47], s[36:37] op_sel_hi:[1,0]
	v_pk_mul_f32 v[48:49], v[48:49], s[36:37] op_sel_hi:[1,0]
	v_pk_mul_f32 v[50:51], v[50:51], s[36:37] op_sel_hi:[1,0]
	v_pk_mul_f32 v[52:53], v[52:53], s[36:37] op_sel_hi:[1,0]
	v_pk_mul_f32 v[54:55], v[54:55], s[36:37] op_sel_hi:[1,0]
	v_pk_mul_f32 v[56:57], v[56:57], s[36:37] op_sel_hi:[1,0]
	v_pk_mul_f32 v[58:59], v[58:59], s[36:37] op_sel_hi:[1,0]
	v_pk_mul_f32 v[60:61], v[60:61], s[36:37] op_sel_hi:[1,0]
	v_pk_mul_f32 v[62:63], v[62:63], s[36:37] op_sel_hi:[1,0]
	v_cvt_pk_fp8_f32 v136, v0, v4
	v_cvt_pk_fp8_f32 v136, v8, v12 op_sel:[0,0,1]
	v_cvt_pk_fp8_f32 v137, v16, v20
	v_cvt_pk_fp8_f32 v137, v24, v28 op_sel:[0,0,1]
	v_cvt_pk_fp8_f32 v138, v32, v36
	v_cvt_pk_fp8_f32 v138, v40, v44 op_sel:[0,0,1]
	v_cvt_pk_fp8_f32 v139, v48, v52
	v_cvt_pk_fp8_f32 v139, v56, v60 op_sel:[0,0,1]
	global_store_dwordx4 v153, v[136:139], s[30:31] sc1
	v_cvt_pk_fp8_f32 v140, v1, v5
	v_cvt_pk_fp8_f32 v140, v9, v13 op_sel:[0,0,1]
	v_cvt_pk_fp8_f32 v141, v17, v21
	v_cvt_pk_fp8_f32 v141, v25, v29 op_sel:[0,0,1]
	v_cvt_pk_fp8_f32 v142, v33, v37
	v_cvt_pk_fp8_f32 v142, v41, v45 op_sel:[0,0,1]
	v_cvt_pk_fp8_f32 v143, v49, v53
	v_cvt_pk_fp8_f32 v143, v57, v61 op_sel:[0,0,1]
	global_store_dwordx4 v153, v[140:143], s[30:31] offset:2048 sc1
	v_cvt_pk_fp8_f32 v144, v2, v6
	v_cvt_pk_fp8_f32 v144, v10, v14 op_sel:[0,0,1]
	v_cvt_pk_fp8_f32 v145, v18, v22
	v_cvt_pk_fp8_f32 v145, v26, v30 op_sel:[0,0,1]
	v_cvt_pk_fp8_f32 v146, v34, v38
	v_cvt_pk_fp8_f32 v146, v42, v46 op_sel:[0,0,1]
	v_cvt_pk_fp8_f32 v147, v50, v54
	v_cvt_pk_fp8_f32 v147, v58, v62 op_sel:[0,0,1]
	global_store_dwordx4 v153, v[144:147], s[34:35] sc1
	v_cvt_pk_fp8_f32 v148, v3, v7
	v_cvt_pk_fp8_f32 v148, v11, v15 op_sel:[0,0,1]
	v_cvt_pk_fp8_f32 v149, v19, v23
	v_cvt_pk_fp8_f32 v149, v27, v31 op_sel:[0,0,1]
	v_cvt_pk_fp8_f32 v150, v35, v39
	v_cvt_pk_fp8_f32 v150, v43, v47 op_sel:[0,0,1]
	v_cvt_pk_fp8_f32 v151, v51, v55
	v_cvt_pk_fp8_f32 v151, v59, v63 op_sel:[0,0,1]
	global_store_dwordx4 v153, v[148:151], s[34:35] offset:2048 sc1
	s_waitcnt vmcnt(4)
	s_lshr_b32 s19, s18, 10
	s_and_b32 s20, s18, 0x3ff
	s_lshr_b32 s21, s20, 6
	s_and_b32 s20, s20, 63
	s_lshl_b32 s22, s19, 22
	s_lshl_b32 s27, s20, 16
	s_add_i32 s22, s22, s27
	s_lshl_b32 s27, s21, 7
	s_add_i32 s22, s22, s27
	s_add_u32 s30, s90, s22
	s_addc_u32 s31, s91, 0
	s_add_u32 s30, s30, 0x3b100000
	s_addc_u32 s31, s31, 0
	s_add_u32 s34, s30, 0x1000
	s_addc_u32 s35, s31, 0
	v_pk_mul_f32 v[64:65], v[64:65], s[36:37] op_sel_hi:[1,0]
	v_pk_mul_f32 v[66:67], v[66:67], s[36:37] op_sel_hi:[1,0]
	v_pk_mul_f32 v[68:69], v[68:69], s[36:37] op_sel_hi:[1,0]
	v_pk_mul_f32 v[70:71], v[70:71], s[36:37] op_sel_hi:[1,0]
	v_pk_mul_f32 v[72:73], v[72:73], s[36:37] op_sel_hi:[1,0]
	v_pk_mul_f32 v[74:75], v[74:75], s[36:37] op_sel_hi:[1,0]
	v_pk_mul_f32 v[76:77], v[76:77], s[36:37] op_sel_hi:[1,0]
	v_pk_mul_f32 v[78:79], v[78:79], s[36:37] op_sel_hi:[1,0]
	v_pk_mul_f32 v[80:81], v[80:81], s[36:37] op_sel_hi:[1,0]
	v_pk_mul_f32 v[82:83], v[82:83], s[36:37] op_sel_hi:[1,0]
	v_pk_mul_f32 v[84:85], v[84:85], s[36:37] op_sel_hi:[1,0]
	v_pk_mul_f32 v[86:87], v[86:87], s[36:37] op_sel_hi:[1,0]
	v_pk_mul_f32 v[88:89], v[88:89], s[36:37] op_sel_hi:[1,0]
	v_pk_mul_f32 v[90:91], v[90:91], s[36:37] op_sel_hi:[1,0]
	v_pk_mul_f32 v[92:93], v[92:93], s[36:37] op_sel_hi:[1,0]
	v_pk_mul_f32 v[94:95], v[94:95], s[36:37] op_sel_hi:[1,0]
	v_pk_mul_f32 v[96:97], v[96:97], s[36:37] op_sel_hi:[1,0]
	v_pk_mul_f32 v[98:99], v[98:99], s[36:37] op_sel_hi:[1,0]
	v_pk_mul_f32 v[100:101], v[100:101], s[36:37] op_sel_hi:[1,0]
	v_pk_mul_f32 v[102:103], v[102:103], s[36:37] op_sel_hi:[1,0]
	v_pk_mul_f32 v[104:105], v[104:105], s[36:37] op_sel_hi:[1,0]
	v_pk_mul_f32 v[106:107], v[106:107], s[36:37] op_sel_hi:[1,0]
	v_pk_mul_f32 v[108:109], v[108:109], s[36:37] op_sel_hi:[1,0]
	v_pk_mul_f32 v[110:111], v[110:111], s[36:37] op_sel_hi:[1,0]
	v_pk_mul_f32 v[112:113], v[112:113], s[36:37] op_sel_hi:[1,0]
	v_pk_mul_f32 v[114:115], v[114:115], s[36:37] op_sel_hi:[1,0]
	v_pk_mul_f32 v[116:117], v[116:117], s[36:37] op_sel_hi:[1,0]
	v_pk_mul_f32 v[118:119], v[118:119], s[36:37] op_sel_hi:[1,0]
	v_pk_mul_f32 v[120:121], v[120:121], s[36:37] op_sel_hi:[1,0]
	v_pk_mul_f32 v[122:123], v[122:123], s[36:37] op_sel_hi:[1,0]
	v_pk_mul_f32 v[124:125], v[124:125], s[36:37] op_sel_hi:[1,0]
	v_pk_mul_f32 v[126:127], v[126:127], s[36:37] op_sel_hi:[1,0]
	v_cvt_pk_fp8_f32 v136, v64, v68
	v_cvt_pk_fp8_f32 v136, v72, v76 op_sel:[0,0,1]
	v_cvt_pk_fp8_f32 v137, v80, v84
	v_cvt_pk_fp8_f32 v137, v88, v92 op_sel:[0,0,1]
	v_cvt_pk_fp8_f32 v138, v96, v100
	v_cvt_pk_fp8_f32 v138, v104, v108 op_sel:[0,0,1]
	v_cvt_pk_fp8_f32 v139, v112, v116
	v_cvt_pk_fp8_f32 v139, v120, v124 op_sel:[0,0,1]
	global_store_dwordx4 v153, v[136:139], s[30:31] sc1
	v_cvt_pk_fp8_f32 v140, v65, v69
	v_cvt_pk_fp8_f32 v140, v73, v77 op_sel:[0,0,1]
	v_cvt_pk_fp8_f32 v141, v81, v85
	v_cvt_pk_fp8_f32 v141, v89, v93 op_sel:[0,0,1]
	v_cvt_pk_fp8_f32 v142, v97, v101
	v_cvt_pk_fp8_f32 v142, v105, v109 op_sel:[0,0,1]
	v_cvt_pk_fp8_f32 v143, v113, v117
	v_cvt_pk_fp8_f32 v143, v121, v125 op_sel:[0,0,1]
	global_store_dwordx4 v153, v[140:143], s[30:31] offset:2048 sc1
	v_cvt_pk_fp8_f32 v144, v66, v70
	v_cvt_pk_fp8_f32 v144, v74, v78 op_sel:[0,0,1]
	v_cvt_pk_fp8_f32 v145, v82, v86
	v_cvt_pk_fp8_f32 v145, v90, v94 op_sel:[0,0,1]
	v_cvt_pk_fp8_f32 v146, v98, v102
	v_cvt_pk_fp8_f32 v146, v106, v110 op_sel:[0,0,1]
	v_cvt_pk_fp8_f32 v147, v114, v118
	v_cvt_pk_fp8_f32 v147, v122, v126 op_sel:[0,0,1]
	global_store_dwordx4 v153, v[144:147], s[34:35] sc1
	v_cvt_pk_fp8_f32 v148, v67, v71
	v_cvt_pk_fp8_f32 v148, v75, v79 op_sel:[0,0,1]
	v_cvt_pk_fp8_f32 v149, v83, v87
	v_cvt_pk_fp8_f32 v149, v91, v95 op_sel:[0,0,1]
	v_cvt_pk_fp8_f32 v150, v99, v103
	v_cvt_pk_fp8_f32 v150, v107, v111 op_sel:[0,0,1]
	v_cvt_pk_fp8_f32 v151, v115, v119
	v_cvt_pk_fp8_f32 v151, v123, v127 op_sel:[0,0,1]
	global_store_dwordx4 v153, v[148:151], s[34:35] offset:2048 sc1
	s_waitcnt vmcnt(0)
	v_mov_b32_e32 v134, v156
	s_branch .LBB0_1051
